# adds: router logits loop fragments requested three k-steps ahead (5 address bases + immediates)
# speedup vs baseline: 1.0345x; 1.0047x over previous
; DI unsigned pk2(float a, float b) { f32x2 v = {a, b}; bf16x2_t r = __builtin_convertvector(v, bf16x2_t); return __builtin_bit_cast(unsigned, r); }
; #define RT_WLOAD(s_, ks_) do { const int k0_ = wave * 256 + (ks_) * 32 + 8 * q; _Pragma("unroll") for (int nt = 0; nt < 5; ++nt) wfr[s_][nt] = *(const bf16x8*)(WRO + (size_t)(nt * 16 + n) * D + k0_); \
;             gfr[s_][0] = *(const f32x4*)(gp + (ks_) * 32); gfr[s_][1] = *(const f32x4*)(gp + (ks_) * 32 + 4); } while (0)
; DI void phase_router(const Args& a, int l, LAS unsigned char* lds, int wave, int lane, int bid, int G, bool dummy = false) {
;     ...
;         RT_WLOAD(0, 0);
; #pragma unroll
;         for (int ks = 0; ks < 8; ++ks) {
;             if (ks < 7) RT_WLOAD((ks + 1) & 1, ks + 1);
;             __builtin_amdgcn_sched_barrier(0);
;             const f32x4 g0 = gfr[ks & 1][0], g1 = gfr[ks & 1][1]; const f32x4 x0 = hv[ks][0], x1 = hv[ks][1];
;             ss += (x0[0] * x0[0] + x0[1] * x0[1]) + (x0[2] * x0[2] + x0[3] * x0[3]) + (x1[0] * x1[0] + x1[1] * x1[1]) + (x1[2] * x1[2] + x1[3] * x1[3]);
;             const f32x4 y0 = x0 * g0, y1 = x1 * g1; hv[ks][0] = y0; hv[ks][1] = y1; u32x4 aw;     aw.x = pk2(y0[0], y0[1]); aw.y = pk2(y0[2], y0[3]); aw.z = pk2(y1[0], y1[1]); aw.w = pk2(y1[2], y1[3]);
;             const bf16x8 af = __builtin_bit_cast(bf16x8, aw);
; #pragma unroll
;             for (int nt = 0; nt < 5; ++nt) acc[nt] = __builtin_amdgcn_mfma_f32_16x16x32_bf16(af, wfr[ks & 1][nt], acc[nt], 0, 0, 0);
;             __builtin_amdgcn_sched_barrier(0); }
.LBB0_1645:
	s_waitcnt vmcnt(0)
	s_barrier
	global_load_dwordx4 v[110:113], v[100:101], off
	global_load_dwordx4 v[114:117], v[102:103], off
	global_load_dwordx4 v[118:121], v[104:105], off
	global_load_dwordx4 v[122:125], v[106:107], off
	global_load_dwordx4 v[126:129], v[108:109], off
	global_load_dwordx4 v[130:133], v[94:95], off
	global_load_dwordx4 v[134:137], v[94:95], off offset:16
	global_load_dwordx4 v[138:141], v[100:101], off offset:64
	global_load_dwordx4 v[142:145], v[102:103], off offset:64
	global_load_dwordx4 v[146:149], v[104:105], off offset:64
	global_load_dwordx4 v[150:153], v[106:107], off offset:64
	global_load_dwordx4 v[154:157], v[108:109], off offset:64
	global_load_dwordx4 v[158:161], v[94:95], off offset:128
	global_load_dwordx4 v[178:181], v[94:95], off offset:144
	global_load_dwordx4 v[182:185], v[100:101], off offset:128
	global_load_dwordx4 v[186:189], v[102:103], off offset:128
	global_load_dwordx4 v[190:193], v[104:105], off offset:128
	global_load_dwordx4 v[194:197], v[106:107], off offset:128
	global_load_dwordx4 v[198:201], v[108:109], off offset:128
	global_load_dwordx4 v[202:205], v[94:95], off offset:256
	global_load_dwordx4 v[206:209], v[94:95], off offset:272
	v_mul_f32_e32 v90, v7, v7
	v_mul_f32_e32 v233, v9, v9
	v_fmac_f32_e32 v90, v6, v6
	v_fmac_f32_e32 v233, v8, v8
	v_add_f32_e32 v90, v90, v233
	v_mul_f32_e32 v233, v3, v3
	v_fmac_f32_e32 v233, v2, v2
	v_add_f32_e32 v90, v233, v90
	v_mul_f32_e32 v233, v5, v5
	v_fmac_f32_e32 v233, v4, v4
	s_waitcnt vmcnt(14)
	v_pk_mul_f32 v[8:9], v[8:9], v[132:133]
	v_pk_mul_f32 v[6:7], v[6:7], v[130:131]
	v_pk_mul_f32 v[4:5], v[4:5], v[136:137]
	v_pk_mul_f32 v[2:3], v[2:3], v[134:135]
	v_cvt_pk_bf16_f32 v164, v6, v7
	v_cvt_pk_bf16_f32 v165, v8, v9
	v_cvt_pk_bf16_f32 v166, v2, v3
	v_cvt_pk_bf16_f32 v167, v4, v5
	v_add_f32_e32 v90, v233, v90
	s_nop 0
	v_mfma_f32_16x16x32_bf16 v[66:69], v[164:167], v[110:113], 0
	v_mfma_f32_16x16x32_bf16 v[78:81], v[164:167], v[114:117], 0
	v_mfma_f32_16x16x32_bf16 v[74:77], v[164:167], v[118:121], 0
	v_mfma_f32_16x16x32_bf16 v[70:73], v[164:167], v[122:125], 0
	v_mfma_f32_16x16x32_bf16 v[82:85], v[164:167], v[126:129], 0
	global_load_dwordx4 v[210:213], v[100:101], off offset:192
	global_load_dwordx4 v[214:217], v[102:103], off offset:192
	global_load_dwordx4 v[234:237], v[104:105], off offset:192
	global_load_dwordx4 v[238:241], v[106:107], off offset:192
	global_load_dwordx4 v[242:245], v[108:109], off offset:192
	global_load_dwordx4 v[246:249], v[94:95], off offset:384
	global_load_dwordx4 v[250:253], v[94:95], off offset:400
	v_mul_f32_e32 v177, v15, v15
	v_mul_f32_e32 v233, v17, v17
	v_fmac_f32_e32 v177, v14, v14
	v_fmac_f32_e32 v233, v16, v16
	v_add_f32_e32 v177, v177, v233
	v_mul_f32_e32 v233, v11, v11
	v_fmac_f32_e32 v233, v10, v10
	v_add_f32_e32 v177, v233, v177
	v_mul_f32_e32 v233, v13, v13
	v_fmac_f32_e32 v233, v12, v12
	s_waitcnt vmcnt(14)
	v_pk_mul_f32 v[16:17], v[16:17], v[160:161]
	v_pk_mul_f32 v[14:15], v[14:15], v[158:159]
	v_pk_mul_f32 v[12:13], v[12:13], v[180:181]
	v_pk_mul_f32 v[10:11], v[10:11], v[178:179]
	v_cvt_pk_bf16_f32 v164, v14, v15
	v_cvt_pk_bf16_f32 v165, v16, v17
	v_cvt_pk_bf16_f32 v166, v10, v11
	v_cvt_pk_bf16_f32 v167, v12, v13
	v_add_f32_e32 v177, v233, v177
	v_add_f32_e32 v90, v177, v90
	v_mfma_f32_16x16x32_bf16 v[66:69], v[164:167], v[138:141], v[66:69]
	v_mfma_f32_16x16x32_bf16 v[78:81], v[164:167], v[142:145], v[78:81]
	v_mfma_f32_16x16x32_bf16 v[74:77], v[164:167], v[146:149], v[74:77]
	v_mfma_f32_16x16x32_bf16 v[70:73], v[164:167], v[150:153], v[70:73]
	v_mfma_f32_16x16x32_bf16 v[82:85], v[164:167], v[154:157], v[82:85]
	global_load_dwordx4 v[110:113], v[100:101], off offset:256
	global_load_dwordx4 v[114:117], v[102:103], off offset:256
	global_load_dwordx4 v[118:121], v[104:105], off offset:256
	global_load_dwordx4 v[122:125], v[106:107], off offset:256
	global_load_dwordx4 v[126:129], v[108:109], off offset:256
	global_load_dwordx4 v[130:133], v[94:95], off offset:512
	global_load_dwordx4 v[134:137], v[94:95], off offset:528
	v_mul_f32_e32 v177, v23, v23
	v_mul_f32_e32 v233, v25, v25
	v_fmac_f32_e32 v177, v22, v22
	v_fmac_f32_e32 v233, v24, v24
	v_add_f32_e32 v177, v177, v233
	v_mul_f32_e32 v233, v19, v19
	v_fmac_f32_e32 v233, v18, v18
	v_add_f32_e32 v177, v233, v177
	v_mul_f32_e32 v233, v21, v21
	v_fmac_f32_e32 v233, v20, v20
	s_waitcnt vmcnt(14)
	v_pk_mul_f32 v[24:25], v[24:25], v[204:205]
	v_pk_mul_f32 v[22:23], v[22:23], v[202:203]
	v_pk_mul_f32 v[20:21], v[20:21], v[208:209]
	v_pk_mul_f32 v[18:19], v[18:19], v[206:207]
	v_cvt_pk_bf16_f32 v164, v22, v23
	v_cvt_pk_bf16_f32 v165, v24, v25
	v_cvt_pk_bf16_f32 v166, v18, v19
	v_cvt_pk_bf16_f32 v167, v20, v21
	v_add_f32_e32 v177, v233, v177
	v_add_f32_e32 v90, v177, v90
	v_mfma_f32_16x16x32_bf16 v[66:69], v[164:167], v[182:185], v[66:69]
	v_mfma_f32_16x16x32_bf16 v[78:81], v[164:167], v[186:189], v[78:81]
	v_mfma_f32_16x16x32_bf16 v[74:77], v[164:167], v[190:193], v[74:77]
	v_mfma_f32_16x16x32_bf16 v[70:73], v[164:167], v[194:197], v[70:73]
	v_mfma_f32_16x16x32_bf16 v[82:85], v[164:167], v[198:201], v[82:85]
	global_load_dwordx4 v[138:141], v[100:101], off offset:320
	global_load_dwordx4 v[142:145], v[102:103], off offset:320
	global_load_dwordx4 v[146:149], v[104:105], off offset:320
	global_load_dwordx4 v[150:153], v[106:107], off offset:320
	global_load_dwordx4 v[154:157], v[108:109], off offset:320
	global_load_dwordx4 v[158:161], v[94:95], off offset:640
	global_load_dwordx4 v[178:181], v[94:95], off offset:656
	v_mul_f32_e32 v177, v31, v31
	v_mul_f32_e32 v233, v33, v33
	v_fmac_f32_e32 v177, v30, v30
	v_fmac_f32_e32 v233, v32, v32
	v_add_f32_e32 v177, v177, v233
	v_mul_f32_e32 v233, v27, v27
	v_fmac_f32_e32 v233, v26, v26
	v_add_f32_e32 v177, v233, v177
	v_mul_f32_e32 v233, v29, v29
	v_fmac_f32_e32 v233, v28, v28
	s_waitcnt vmcnt(14)
; DI unsigned pk2(float a, float b) { f32x2 v = {a, b}; bf16x2_t r = __builtin_convertvector(v, bf16x2_t); return __builtin_bit_cast(unsigned, r); }
; #define RT_WLOAD(s_, ks_) do { const int k0_ = wave * 256 + (ks_) * 32 + 8 * q; _Pragma("unroll") for (int nt = 0; nt < 5; ++nt) wfr[s_][nt] = *(const bf16x8*)(WRO + (size_t)(nt * 16 + n) * D + k0_); \
;             gfr[s_][0] = *(const f32x4*)(gp + (ks_) * 32); gfr[s_][1] = *(const f32x4*)(gp + (ks_) * 32 + 4); } while (0)
; DI void phase_router(const Args& a, int l, LAS unsigned char* lds, int wave, int lane, int bid, int G, bool dummy = false) {
;     ...
; #pragma unroll
;         for (int ks = 0; ks < 8; ++ks) {
;             if (ks < 7) RT_WLOAD((ks + 1) & 1, ks + 1);
;             __builtin_amdgcn_sched_barrier(0);
;             const f32x4 g0 = gfr[ks & 1][0], g1 = gfr[ks & 1][1]; const f32x4 x0 = hv[ks][0], x1 = hv[ks][1];
;             ss += (x0[0] * x0[0] + x0[1] * x0[1]) + (x0[2] * x0[2] + x0[3] * x0[3]) + (x1[0] * x1[0] + x1[1] * x1[1]) + (x1[2] * x1[2] + x1[3] * x1[3]);
;             const f32x4 y0 = x0 * g0, y1 = x1 * g1; hv[ks][0] = y0; hv[ks][1] = y1; u32x4 aw;     aw.x = pk2(y0[0], y0[1]); aw.y = pk2(y0[2], y0[3]); aw.z = pk2(y1[0], y1[1]); aw.w = pk2(y1[2], y1[3]);
;             const bf16x8 af = __builtin_bit_cast(bf16x8, aw);
; #pragma unroll
;             for (int nt = 0; nt < 5; ++nt) acc[nt] = __builtin_amdgcn_mfma_f32_16x16x32_bf16(af, wfr[ks & 1][nt], acc[nt], 0, 0, 0);
;             __builtin_amdgcn_sched_barrier(0); }
;     ...
;         ss += __shfl_xor(ss, 16); ss += __shfl_xor(ss, 32);
;         if (q == 0) ssp[wave * 16 + n] = ss;
	v_pk_mul_f32 v[32:33], v[32:33], v[248:249]
	v_pk_mul_f32 v[30:31], v[30:31], v[246:247]
	v_pk_mul_f32 v[28:29], v[28:29], v[252:253]
	v_pk_mul_f32 v[26:27], v[26:27], v[250:251]
	v_cvt_pk_bf16_f32 v164, v30, v31
	v_cvt_pk_bf16_f32 v165, v32, v33
	v_cvt_pk_bf16_f32 v166, v26, v27
	v_cvt_pk_bf16_f32 v167, v28, v29
	v_add_f32_e32 v177, v233, v177
	v_add_f32_e32 v90, v177, v90
	v_mfma_f32_16x16x32_bf16 v[66:69], v[164:167], v[210:213], v[66:69]
	v_mfma_f32_16x16x32_bf16 v[78:81], v[164:167], v[214:217], v[78:81]
	v_mfma_f32_16x16x32_bf16 v[74:77], v[164:167], v[234:237], v[74:77]
	v_mfma_f32_16x16x32_bf16 v[70:73], v[164:167], v[238:241], v[70:73]
	v_mfma_f32_16x16x32_bf16 v[82:85], v[164:167], v[242:245], v[82:85]
	global_load_dwordx4 v[182:185], v[100:101], off offset:384
	global_load_dwordx4 v[186:189], v[102:103], off offset:384
	global_load_dwordx4 v[190:193], v[104:105], off offset:384
	global_load_dwordx4 v[194:197], v[106:107], off offset:384
	global_load_dwordx4 v[198:201], v[108:109], off offset:384
	global_load_dwordx4 v[202:205], v[94:95], off offset:768
	global_load_dwordx4 v[206:209], v[94:95], off offset:784
	v_mul_f32_e32 v177, v39, v39
	v_mul_f32_e32 v233, v41, v41
	v_fmac_f32_e32 v177, v38, v38
	v_fmac_f32_e32 v233, v40, v40
	v_add_f32_e32 v177, v177, v233
	v_mul_f32_e32 v233, v35, v35
	v_fmac_f32_e32 v233, v34, v34
	v_add_f32_e32 v177, v233, v177
	v_mul_f32_e32 v233, v37, v37
	v_fmac_f32_e32 v233, v36, v36
	s_waitcnt vmcnt(14)
	v_pk_mul_f32 v[40:41], v[40:41], v[132:133]
	v_pk_mul_f32 v[38:39], v[38:39], v[130:131]
	v_pk_mul_f32 v[36:37], v[36:37], v[136:137]
	v_pk_mul_f32 v[34:35], v[34:35], v[134:135]
	v_cvt_pk_bf16_f32 v164, v38, v39
	v_cvt_pk_bf16_f32 v165, v40, v41
	v_cvt_pk_bf16_f32 v166, v34, v35
	v_cvt_pk_bf16_f32 v167, v36, v37
	v_add_f32_e32 v177, v233, v177
	v_add_f32_e32 v90, v177, v90
	v_mfma_f32_16x16x32_bf16 v[66:69], v[164:167], v[110:113], v[66:69]
	v_mfma_f32_16x16x32_bf16 v[78:81], v[164:167], v[114:117], v[78:81]
	v_mfma_f32_16x16x32_bf16 v[74:77], v[164:167], v[118:121], v[74:77]
	v_mfma_f32_16x16x32_bf16 v[70:73], v[164:167], v[122:125], v[70:73]
	v_mfma_f32_16x16x32_bf16 v[82:85], v[164:167], v[126:129], v[82:85]
	global_load_dwordx4 v[210:213], v[100:101], off offset:448
	global_load_dwordx4 v[214:217], v[102:103], off offset:448
	global_load_dwordx4 v[234:237], v[104:105], off offset:448
	global_load_dwordx4 v[238:241], v[106:107], off offset:448
	global_load_dwordx4 v[242:245], v[108:109], off offset:448
	global_load_dwordx4 v[246:249], v[94:95], off offset:896
	global_load_dwordx4 v[250:253], v[94:95], off offset:912
	v_mul_f32_e32 v177, v47, v47
	v_mul_f32_e32 v233, v49, v49
	v_fmac_f32_e32 v177, v46, v46
	v_fmac_f32_e32 v233, v48, v48
	v_add_f32_e32 v177, v177, v233
	v_mul_f32_e32 v233, v43, v43
	v_fmac_f32_e32 v233, v42, v42
	v_add_f32_e32 v177, v233, v177
	v_mul_f32_e32 v233, v45, v45
	v_fmac_f32_e32 v233, v44, v44
	s_waitcnt vmcnt(14)
	v_pk_mul_f32 v[48:49], v[48:49], v[160:161]
	v_pk_mul_f32 v[46:47], v[46:47], v[158:159]
	v_pk_mul_f32 v[44:45], v[44:45], v[180:181]
	v_pk_mul_f32 v[42:43], v[42:43], v[178:179]
	v_cvt_pk_bf16_f32 v164, v46, v47
	v_cvt_pk_bf16_f32 v165, v48, v49
	v_cvt_pk_bf16_f32 v166, v42, v43
	v_cvt_pk_bf16_f32 v167, v44, v45
	v_add_f32_e32 v177, v233, v177
	v_add_f32_e32 v90, v177, v90
	v_mfma_f32_16x16x32_bf16 v[66:69], v[164:167], v[138:141], v[66:69]
	v_mfma_f32_16x16x32_bf16 v[78:81], v[164:167], v[142:145], v[78:81]
	v_mfma_f32_16x16x32_bf16 v[74:77], v[164:167], v[146:149], v[74:77]
	v_mfma_f32_16x16x32_bf16 v[70:73], v[164:167], v[150:153], v[70:73]
	v_mfma_f32_16x16x32_bf16 v[82:85], v[164:167], v[154:157], v[82:85]
	v_mul_f32_e32 v177, v65, v65
	v_fmac_f32_e32 v177, v64, v64
	v_mul_f32_e32 v233, v59, v59
	v_fmac_f32_e32 v233, v58, v58
	v_mul_f32_e32 v162, v61, v61
	v_fmac_f32_e32 v162, v60, v60
	v_mul_f32_e32 v163, v63, v63
	v_add_f32_e32 v233, v233, v162
	v_fmac_f32_e32 v163, v62, v62
	v_add_f32_e32 v172, v163, v233
	v_add_f32_e32 v172, v177, v172
	v_add_f32_e32 v90, v172, v90
	s_waitcnt vmcnt(7)
	v_pk_mul_f32 v[60:61], v[60:61], v[204:205]
	v_pk_mul_f32 v[58:59], v[58:59], v[202:203]
	v_pk_mul_f32 v[64:65], v[64:65], v[208:209]
	v_pk_mul_f32 v[62:63], v[62:63], v[206:207]
	v_cvt_pk_bf16_f32 v164, v58, v59
	v_cvt_pk_bf16_f32 v165, v60, v61
	v_cvt_pk_bf16_f32 v166, v62, v63
	v_cvt_pk_bf16_f32 v167, v64, v65
	s_nop 0
	s_nop 0
	v_mfma_f32_16x16x32_bf16 v[66:69], v[164:167], v[182:185], v[66:69]
	v_mfma_f32_16x16x32_bf16 v[78:81], v[164:167], v[186:189], v[78:81]
	v_mfma_f32_16x16x32_bf16 v[74:77], v[164:167], v[190:193], v[74:77]
	v_mfma_f32_16x16x32_bf16 v[70:73], v[164:167], v[194:197], v[70:73]
	v_mfma_f32_16x16x32_bf16 v[82:85], v[164:167], v[198:201], v[82:85]
	v_mul_f32_e32 v177, v55, v55
	v_mul_f32_e32 v233, v57, v57
	v_fmac_f32_e32 v177, v54, v54
	v_fmac_f32_e32 v233, v56, v56
	v_add_f32_e32 v177, v177, v233
	v_mul_f32_e32 v233, v51, v51
	v_fmac_f32_e32 v233, v50, v50
	v_add_f32_e32 v177, v233, v177
	v_mul_f32_e32 v233, v53, v53
	v_fmac_f32_e32 v233, v52, v52
	s_waitcnt vmcnt(0)
	v_pk_mul_f32 v[56:57], v[56:57], v[248:249]
	v_pk_mul_f32 v[54:55], v[54:55], v[246:247]
	v_pk_mul_f32 v[52:53], v[52:53], v[252:253]
	v_pk_mul_f32 v[50:51], v[50:51], v[250:251]
	v_cvt_pk_bf16_f32 v164, v54, v55
	v_cvt_pk_bf16_f32 v165, v56, v57
	v_cvt_pk_bf16_f32 v166, v50, v51
	v_cvt_pk_bf16_f32 v167, v52, v53
	v_add_f32_e32 v177, v233, v177
	v_add_f32_e32 v90, v177, v90
	v_mfma_f32_16x16x32_bf16 v[66:69], v[164:167], v[210:213], v[66:69]
	v_mfma_f32_16x16x32_bf16 v[78:81], v[164:167], v[214:217], v[78:81]
	v_mfma_f32_16x16x32_bf16 v[74:77], v[164:167], v[234:237], v[74:77]
	v_mfma_f32_16x16x32_bf16 v[70:73], v[164:167], v[238:241], v[70:73]
	v_mfma_f32_16x16x32_bf16 v[82:85], v[164:167], v[242:245], v[82:85]
	ds_bpermute_b32 v164, v87, v90
	s_waitcnt lgkmcnt(0)
	v_add_f32_e32 v90, v90, v164
	ds_bpermute_b32 v177, v174, v90
	s_and_saveexec_b64 s[2:3], s[38:39]
	s_cbranch_execz .LBB0_1647
	s_waitcnt lgkmcnt(0)
	v_add_f32_e32 v90, v90, v177
	ds_write_b32 v175, v90 offset:40960
